# baseline (speedup 1.0000x reference)
_Z11attn_kernelPKDF16_S0_S0_PKjPf:
	s_and_b32 s27, s2, 7
	s_lshr_b32 s3, s2, 3
	s_lshr_b32 s12, s2, 6
	v_readfirstlane_b32 s23, v0
	s_mov_b32 s13, 0
	s_lshl_b32 s2, s2, 5
	s_load_dwordx8 s[4:11], s[0:1], 0x0
	s_and_b32 s28, s3, 0x1ffffff8
	s_lshr_b32 s20, s23, 6
	s_lshl_b64 s[14:15], s[12:13], 11
	s_and_b32 s2, s2, 0x700
	s_or_b32 s16, s28, s27
	s_or_b32 s2, s14, s2
	s_lshl_b32 s3, s20, 5
	s_add_u32 s2, s2, s3
	s_addc_u32 s3, s15, 0
	s_lshl_b64 s[14:15], s[2:3], 10
	s_waitcnt lgkmcnt(0)
	s_add_u32 s4, s4, s14
	s_addc_u32 s5, s5, s15
	s_lshl_b32 s12, s27, 7
	s_add_u32 s4, s4, s12
	s_mov_b32 s17, s13
	s_addc_u32 s5, s5, 0
	s_lshl_b64 s[12:13], s[16:17], 18
	s_add_u32 s14, s6, s12
	s_addc_u32 s15, s7, s13
	s_add_u32 s12, s8, s12
	s_addc_u32 s13, s9, s13
	s_lshl_b32 s22, s20, 10
	s_cmp_lg_u32 0, -1
	v_and_b32_e32 v1, 63, v0
	s_cselect_b32 s6, 0, 0
	v_lshl_or_b32 v189, v1, 4, s22
	s_add_i32 s24, s22, s6
	s_mov_b32 s6, m0
	s_mov_b32 m0, s24
	s_nop 0
	global_load_lds_dwordx4 v189, s[14:15]
	s_mov_b32 m0, s6
	v_bfe_u32 v18, v0, 5, 1
	s_add_i32 s25, s24, 0x6000
	s_mov_b32 s6, m0
	s_mov_b32 m0, s25
	s_nop 0
	global_load_lds_dwordx4 v189, s[12:13]
	s_mov_b32 m0, s6
	v_and_b32_e32 v181, 31, v0
	s_add_u32 s6, s14, 0x2000
	v_lshlrev_b32_e32 v184, 4, v18
	s_addc_u32 s7, s15, 0
	s_add_i32 s17, s24, 0x2000
	s_mov_b32 s18, m0
	s_mov_b32 m0, s17
	s_nop 0
	global_load_lds_dwordx4 v189, s[6:7]
	s_mov_b32 m0, s18
	v_lshl_or_b32 v2, v181, 10, v184
	global_load_dwordx4 v[124:127], v2, s[4:5]
	global_load_dwordx4 v[120:123], v2, s[4:5] offset:32
	global_load_dwordx4 v[116:119], v2, s[4:5] offset:64
	global_load_dwordx4 v[112:115], v2, s[4:5] offset:96
	v_lshlrev_b32_e32 v182, 10, v18
	v_lshlrev_b32_e32 v19, 4, v181
	v_add3_u32 v190, 0, v182, v19
	s_lshl_b32 s5, s16, 2
	s_load_dword s5, s[10:11], s5 offset:0x0
	s_mov_b32 s4, 0x42a20000
	v_mov_b32_e32 v2, 0
	v_mov_b32_e32 v3, v2
	v_mov_b32_e32 v4, v2
	v_mov_b32_e32 v5, v2
	v_mov_b32_e32 v6, v2
	v_mov_b32_e32 v7, v2
	v_mov_b32_e32 v8, v2
	v_mov_b32_e32 v9, v2
	v_mov_b32_e32 v10, v2
	v_mov_b32_e32 v11, v2
	v_mov_b32_e32 v12, v2
	v_mov_b32_e32 v13, v2
	v_mov_b32_e32 v14, v2
	v_mov_b32_e32 v15, v2
	v_mov_b32_e32 v16, v2
	v_mov_b32_e32 v17, v2
	s_waitcnt vmcnt(3)
	v_fma_mix_f32 v19, v124, v124, 0 op_sel_hi:[1,1,0]
	s_nop 0
	v_fma_mix_f32 v19, v124, v124, v19 op_sel:[1,1,0] op_sel_hi:[1,1,0]
	s_nop 0
	v_fma_mix_f32 v19, v125, v125, v19 op_sel_hi:[1,1,0]
	s_nop 0
	v_fma_mix_f32 v19, v125, v125, v19 op_sel:[1,1,0] op_sel_hi:[1,1,0]
	s_nop 0
	v_fma_mix_f32 v19, v126, v126, v19 op_sel_hi:[1,1,0]
	s_nop 0
	v_fma_mix_f32 v19, v126, v126, v19 op_sel:[1,1,0] op_sel_hi:[1,1,0]
	s_nop 0
	v_fma_mix_f32 v19, v127, v127, v19 op_sel_hi:[1,1,0]
	s_nop 0
	v_fma_mix_f32 v19, v127, v127, v19 op_sel:[1,1,0] op_sel_hi:[1,1,0]
	s_waitcnt vmcnt(2)
	v_fma_mix_f32 v19, v120, v120, v19 op_sel_hi:[1,1,0]
	s_nop 0
	v_fma_mix_f32 v19, v120, v120, v19 op_sel:[1,1,0] op_sel_hi:[1,1,0]
	s_nop 0
	v_fma_mix_f32 v19, v121, v121, v19 op_sel_hi:[1,1,0]
	s_nop 0
	v_fma_mix_f32 v19, v121, v121, v19 op_sel:[1,1,0] op_sel_hi:[1,1,0]
	s_nop 0
	v_fma_mix_f32 v19, v122, v122, v19 op_sel_hi:[1,1,0]
	s_nop 0
	v_fma_mix_f32 v19, v122, v122, v19 op_sel:[1,1,0] op_sel_hi:[1,1,0]
	s_nop 0
	v_fma_mix_f32 v19, v123, v123, v19 op_sel_hi:[1,1,0]
	s_nop 0
	v_fma_mix_f32 v19, v123, v123, v19 op_sel:[1,1,0] op_sel_hi:[1,1,0]
	s_waitcnt vmcnt(1)
	v_fma_mix_f32 v19, v116, v116, v19 op_sel_hi:[1,1,0]
	s_nop 0
	v_fma_mix_f32 v19, v116, v116, v19 op_sel:[1,1,0] op_sel_hi:[1,1,0]
	s_nop 0
	v_fma_mix_f32 v19, v117, v117, v19 op_sel_hi:[1,1,0]
	s_nop 0
	v_fma_mix_f32 v19, v117, v117, v19 op_sel:[1,1,0] op_sel_hi:[1,1,0]
	s_nop 0
	v_fma_mix_f32 v19, v118, v118, v19 op_sel_hi:[1,1,0]
	s_nop 0
	v_fma_mix_f32 v19, v118, v118, v19 op_sel:[1,1,0] op_sel_hi:[1,1,0]
	s_nop 0
	v_fma_mix_f32 v19, v119, v119, v19 op_sel_hi:[1,1,0]
	s_nop 0
	v_fma_mix_f32 v19, v119, v119, v19 op_sel:[1,1,0] op_sel_hi:[1,1,0]
	s_waitcnt vmcnt(0)
	v_fma_mix_f32 v19, v112, v112, v19 op_sel_hi:[1,1,0]
	s_nop 0
	v_fma_mix_f32 v19, v112, v112, v19 op_sel:[1,1,0] op_sel_hi:[1,1,0]
	s_nop 0
	v_fma_mix_f32 v19, v113, v113, v19 op_sel_hi:[1,1,0]
	s_nop 0
	v_fma_mix_f32 v19, v113, v113, v19 op_sel:[1,1,0] op_sel_hi:[1,1,0]
	s_nop 0
	v_fma_mix_f32 v19, v114, v114, v19 op_sel_hi:[1,1,0]
	s_nop 0
	v_fma_mix_f32 v19, v114, v114, v19 op_sel:[1,1,0] op_sel_hi:[1,1,0]
	s_nop 0
	v_fma_mix_f32 v19, v115, v115, v19 op_sel_hi:[1,1,0]
	s_nop 0
	v_fma_mix_f32 v19, v115, v115, v19 op_sel:[1,1,0] op_sel_hi:[1,1,0]
	s_nop 0
	v_mov_b32_e32 v20, v19
	s_nop 1
	v_permlane32_swap_b32_e32 v19, v20
	v_add_f32_e32 v19, v19, v20
	s_waitcnt lgkmcnt(0)
	v_mul_f32_e32 v19, s5, v19
	v_cmp_ge_f32_e32 vcc, s4, v19
	s_cmp_eq_u64 vcc, exec
	s_cselect_b64 s[4:5], -1, 0
	s_add_u32 s6, s14, 0x4000
	s_addc_u32 s7, s15, 0
	s_add_i32 s10, s24, 0x4000
	s_mov_b32 s11, m0
	s_mov_b32 m0, s10
	s_nop 0
	global_load_lds_dwordx4 v189, s[6:7]
	s_mov_b32 m0, s11
	s_waitcnt vmcnt(3) lgkmcnt(0)
	s_barrier
	ds_read_b128 v[20:23], v190
	ds_read_b128 v[24:27], v190 offset:512
	s_waitcnt lgkmcnt(1)
	v_mfma_f32_32x32x16_f16 v[96:111], v[20:23], v[124:127], v[2:17]
	v_cndmask_b32_e64 v19, 0, 1, s[4:5]
	s_nop 0
	v_readfirstlane_b32 s4, v19
	s_bitcmp1_b32 s4, 0
	s_cselect_b64 s[16:17], -1, 0
	s_xor_b64 s[18:19], s[16:17], -1
	s_mov_b64 s[4:5], -1
	s_waitcnt lgkmcnt(0)
	v_mfma_f32_32x32x16_f16 v[80:95], v[24:27], v[124:127], v[2:17]
	ds_read_b128 v[20:23], v190 offset:2048
	ds_read_b128 v[24:27], v190 offset:2560
	s_and_b64 vcc, exec, s[18:19]
	s_waitcnt lgkmcnt(1)
	v_mfma_f32_32x32x16_f16 v[96:111], v[20:23], v[120:123], v[96:111]
	s_waitcnt lgkmcnt(0)
	v_mfma_f32_32x32x16_f16 v[80:95], v[24:27], v[120:123], v[80:95]
	ds_read_b128 v[20:23], v190 offset:4096
	ds_read_b128 v[24:27], v190 offset:4608
	s_waitcnt lgkmcnt(1)
	v_mfma_f32_32x32x16_f16 v[96:111], v[20:23], v[116:119], v[96:111]
	s_waitcnt lgkmcnt(0)
	v_mfma_f32_32x32x16_f16 v[80:95], v[24:27], v[116:119], v[80:95]
	ds_read_b128 v[20:23], v190 offset:6144
	ds_read_b128 v[24:27], v190 offset:6656
	s_waitcnt lgkmcnt(1)
	v_mfma_f32_32x32x16_f16 v[96:111], v[20:23], v[112:115], v[96:111]
	s_waitcnt lgkmcnt(0)
	v_mfma_f32_32x32x16_f16 v[80:95], v[24:27], v[112:115], v[80:95]
	s_cbranch_vccz .LBB2_2
	v_max3_f32 v19, v96, v97, v80
	v_max3_f32 v20, v98, v99, v81
	s_nop 0
	v_max3_f32 v19, v19, v82, v83
	v_max3_f32 v20, v20, v102, v103
	s_nop 0
	v_max3_f32 v19, v19, v100, v101
	v_max3_f32 v20, v20, v86, v87
	s_nop 0
	v_max3_f32 v19, v19, v84, v85
	v_max3_f32 v20, v20, v106, v107
	s_nop 0
	v_max3_f32 v19, v19, v104, v105
	v_max3_f32 v20, v20, v90, v91
	s_nop 0
	v_max3_f32 v19, v19, v88, v89
	v_max3_f32 v20, v20, v110, v111
	s_nop 0
	v_max3_f32 v19, v19, v108, v109
	v_max3_f32 v20, v20, v94, v95
	s_nop 0
	v_max3_f32 v19, v19, v92, v93
	s_nop 0
	v_max_f32 v19, v19, v20
	s_nop 0
	v_mov_b32_e32 v20, v19
	s_nop 1
	v_permlane32_swap_b32_e32 v19, v20
	v_max_f32 v180, v19, v20
	s_nop 0
	v_sub_f32_e32 v19, v96, v180
	v_exp_f32_e32 v64, v19
	v_sub_f32_e32 v19, v80, v180
	v_exp_f32_e32 v48, v19
	v_sub_f32_e32 v19, v97, v180
	v_exp_f32_e32 v65, v19
	v_sub_f32_e32 v19, v81, v180
	v_exp_f32_e32 v49, v19
	v_sub_f32_e32 v19, v98, v180
	v_exp_f32_e32 v66, v19
	v_sub_f32_e32 v19, v82, v180
	v_exp_f32_e32 v50, v19
	v_sub_f32_e32 v19, v99, v180
	v_exp_f32_e32 v67, v19
	v_sub_f32_e32 v19, v83, v180
	v_exp_f32_e32 v51, v19
	v_sub_f32_e32 v19, v100, v180
	v_exp_f32_e32 v68, v19
	v_sub_f32_e32 v19, v84, v180
	v_exp_f32_e32 v52, v19
	v_sub_f32_e32 v19, v101, v180
	v_exp_f32_e32 v69, v19
	v_sub_f32_e32 v53, v85, v180
	v_sub_f32_e32 v19, v102, v180
	v_exp_f32_e32 v70, v19
	v_sub_f32_e32 v54, v86, v180
	v_sub_f32_e32 v19, v103, v180
	v_exp_f32_e32 v71, v19
	v_sub_f32_e32 v55, v87, v180
	v_sub_f32_e32 v19, v104, v180
	v_exp_f32_e32 v72, v19
	v_sub_f32_e32 v19, v105, v180
	v_exp_f32_e32 v73, v19
	v_sub_f32_e32 v19, v106, v180
	v_exp_f32_e32 v74, v19
	v_sub_f32_e32 v19, v107, v180
	v_exp_f32_e32 v75, v19
	v_sub_f32_e32 v19, v108, v180
	v_exp_f32_e32 v76, v19
	v_sub_f32_e32 v19, v109, v180
	v_exp_f32_e32 v77, v19
	v_sub_f32_e32 v19, v110, v180
	v_xor_b32_e32 v32, 0x80000000, v180
	v_exp_f32_e32 v78, v19
	v_sub_f32_e32 v19, v111, v180
	v_mov_b32_e32 v33, v32
	v_mov_b32_e32 v34, v32
	v_mov_b32_e32 v35, v32
	v_mov_b32_e32 v36, v32
	v_mov_b32_e32 v37, v32
	v_mov_b32_e32 v38, v32
	v_mov_b32_e32 v39, v32
	v_mov_b32_e32 v40, v32
	v_mov_b32_e32 v41, v32
	v_mov_b32_e32 v42, v32
	v_mov_b32_e32 v43, v32
	v_mov_b32_e32 v44, v32
	v_mov_b32_e32 v45, v32
	v_mov_b32_e32 v46, v32
	v_mov_b32_e32 v47, v32
	v_pk_add_f32 v[56:57], v[88:89], v[180:181] op_sel_hi:[1,0] neg_lo:[0,1] neg_hi:[0,1]
	v_pk_add_f32 v[58:59], v[90:91], v[180:181] op_sel_hi:[1,0] neg_lo:[0,1] neg_hi:[0,1]
	v_pk_add_f32 v[60:61], v[92:93], v[180:181] op_sel_hi:[1,0] neg_lo:[0,1] neg_hi:[0,1]
	v_exp_f32_e32 v79, v19
	v_pk_add_f32 v[62:63], v[94:95], v[180:181] op_sel_hi:[1,0] neg_lo:[0,1] neg_hi:[0,1]
	s_load_dwordx2 s[6:7], s[0:1], 0x20
	s_lshl_b32 s21, s27, 6
	s_cbranch_execz .LBB2_3
	s_branch .LBB2_4

.LBB2_3:
	s_nop 6
	v_exp_f32_e32 v80, v80
	v_exp_f32_e32 v81, v81
	v_exp_f32_e32 v82, v82
	v_exp_f32_e32 v83, v83
	v_exp_f32_e32 v84, v84
	v_exp_f32_e32 v64, v96
	v_exp_f32_e32 v65, v97
	v_exp_f32_e32 v66, v98
	v_exp_f32_e32 v67, v99
	v_exp_f32_e32 v68, v100
	v_exp_f32_e32 v69, v101
	v_exp_f32_e32 v70, v102
	v_exp_f32_e32 v71, v103
	v_exp_f32_e32 v72, v104
	v_exp_f32_e32 v73, v105
	v_exp_f32_e32 v74, v106
	v_exp_f32_e32 v75, v107
	v_exp_f32_e32 v76, v108
	v_exp_f32_e32 v77, v109
	v_exp_f32_e32 v78, v110
	v_exp_f32_e32 v79, v111
	v_mov_b64_e32 v[48:49], v[80:81]
	v_mov_b64_e32 v[46:47], v[16:17]
	v_mov_b32_e32 v180, 0
	v_mov_b64_e32 v[50:51], v[82:83]
	v_mov_b64_e32 v[52:53], v[84:85]
	v_mov_b64_e32 v[54:55], v[86:87]
	v_mov_b64_e32 v[56:57], v[88:89]
	v_mov_b64_e32 v[58:59], v[90:91]
	v_mov_b64_e32 v[60:61], v[92:93]
	v_mov_b64_e32 v[62:63], v[94:95]
	v_mov_b64_e32 v[44:45], v[14:15]
	v_mov_b64_e32 v[42:43], v[12:13]
	v_mov_b64_e32 v[40:41], v[10:11]
	v_mov_b64_e32 v[38:39], v[8:9]
	v_mov_b64_e32 v[36:37], v[6:7]
	v_mov_b64_e32 v[34:35], v[4:5]
	v_mov_b64_e32 v[32:33], v[2:3]

.Lattn_prio_done:
.LBB2_5:
	s_add_i32 s26, s26, 2
	v_add_u32_e32 v191, s3, v187
	ds_read_b64_tr_b16 v[176:177], v191 offset:24576
	ds_read_b64_tr_b16 v[178:179], v191 offset:25088
	v_mfma_f32_32x32x16_f16 v[96:111], v[172:175], v[124:127], v[32:47]
	v_exp_f32_e32 v56, v56
	v_exp_f32_e32 v57, v57
	v_cvt_pk_f16_f32 v140, v64, v65
	v_cvt_pk_f16_f32 v141, v66, v67
	ds_read_b64_tr_b16 v[172:173], v191 offset:28672
	ds_read_b64_tr_b16 v[174:175], v191 offset:29184
	v_mfma_f32_32x32x16_f16 v[80:95], v[168:171], v[124:127], v[32:47]
	v_exp_f32_e32 v58, v58
	v_exp_f32_e32 v59, v59
	v_pk_add_f16 v128, v140, v141
	v_cvt_pk_f16_f32 v142, v68, v69
	v_cvt_pk_f16_f32 v143, v70, v71
	ds_read_b64_tr_b16 v[64:65], v191 offset:25600
	ds_read_b64_tr_b16 v[66:67], v191 offset:26112
	v_mfma_f32_32x32x16_f16 v[96:111], v[164:167], v[120:123], v[96:111]
	v_exp_f32_e32 v60, v60
	v_exp_f32_e32 v61, v61
	v_pk_add_f16 v129, v142, v143
	v_cvt_pk_f16_f32 v136, v72, v73
	v_cvt_pk_f16_f32 v137, v74, v75
	ds_read_b64_tr_b16 v[68:69], v191 offset:29696
	ds_read_b64_tr_b16 v[70:71], v191 offset:30208
	v_mfma_f32_32x32x16_f16 v[80:95], v[160:163], v[120:123], v[80:95]
	v_exp_f32_e32 v62, v62
	v_exp_f32_e32 v63, v63
	v_pk_add_f16 v72, v136, v137
	v_pk_add_f16 v128, v128, v129
	v_cvt_pk_f16_f32 v138, v76, v77
	v_cvt_pk_f16_f32 v139, v78, v79
	s_min_u32 s2, s26, 28
	s_lshl_b32 s2, s2, 13
	s_add_u32 s2, s14, s2
	s_addc_u32 s3, s15, 0
	s_add_u32 s2, s2, 0x6000
	s_addc_u32 s3, s3, 0
	s_add_i32 s4, s31, s24
	s_mov_b32 s5, m0
	s_mov_b32 m0, s4
	s_nop 0
	global_load_lds_dwordx4 v189, s[2:3]
	s_mov_b32 m0, s5
	ds_read_b64_tr_b16 v[76:77], v191 offset:26624
	ds_read_b64_tr_b16 v[78:79], v191 offset:27136
	v_mfma_f32_32x32x16_f16 v[96:111], v[156:159], v[116:119], v[96:111]
	v_pk_add_f16 v73, v138, v139
	v_cvt_pk_f16_f32 v132, v48, v49
	v_cvt_pk_f16_f32 v133, v50, v51
	v_exp_f32_e32 v53, v53
	v_exp_f32_e32 v54, v54
	ds_read_b64_tr_b16 v[48:49], v191 offset:30720
	ds_read_b64_tr_b16 v[50:51], v191 offset:31232
	v_mfma_f32_32x32x16_f16 v[80:95], v[152:155], v[116:119], v[80:95]
	v_exp_f32_e32 v55, v55
	v_pk_add_f16 v129, v72, v73
	v_cvt_pk_f16_f32 v134, v52, v53
	v_cvt_pk_f16_f32 v135, v54, v55
	v_pk_add_f16 v156, v132, v133
	s_add_u32 s2, s27, 0x2000
	s_addc_u32 s3, s28, 0
	s_add_i32 s4, s29, s25
	s_mov_b32 s5, m0
	s_mov_b32 m0, s4
	s_nop 0
	global_load_lds_dwordx4 v189, s[2:3]
	s_mov_b32 m0, s5
	ds_read_b64_tr_b16 v[72:73], v191 offset:27648
	ds_read_b64_tr_b16 v[74:75], v191 offset:28160
	v_mfma_f32_32x32x16_f16 v[96:111], v[148:151], v[112:115], v[96:111]
	v_pk_add_f16 v153, v128, v129
	v_cvt_pk_f16_f32 v128, v56, v57
	v_cvt_pk_f16_f32 v129, v58, v59
	v_pk_add_f16 v152, v134, v135
	ds_read_b64_tr_b16 v[52:53], v191 offset:31744
	ds_read_b64_tr_b16 v[54:55], v191 offset:32256
	v_mfma_f32_32x32x16_f16 v[80:95], v[144:147], v[112:115], v[80:95]
	v_pk_add_f16 v56, v128, v129
	v_pk_add_f16 v57, v156, v152
	v_cvt_pk_f16_f32 v130, v60, v61
	v_cvt_pk_f16_f32 v131, v62, v63
	s_andn2_b64 vcc, exec, s[18:19]
	v_pk_add_f16 v57, v153, v57
	v_pk_add_f16 v58, v130, v131
	s_cbranch_vccnz .LBB2_7
	v_pk_add_f16 v59, v56, v58
	v_max3_f32 v61, v96, v97, v80
	v_max3_f32 v62, v98, v99, v81
	s_mov_b64 s[8:9], 0
	v_pk_add_f16 v59, v57, v59
	s_nop 0
	v_cvt_f32_f16_e32 v60, v59
	v_cvt_f32_f16_sdwa v59, v59 dst_sel:DWORD dst_unused:UNUSED_PAD src0_sel:WORD_1
	v_add_f32_e32 v59, v59, v60
	v_add_f32_e32 v188, v188, v59
	v_max3_f32 v59, v61, v82, v83
	v_max3_f32 v60, v62, v102, v103
	s_nop 0
	v_max3_f32 v59, v59, v100, v101
	v_max3_f32 v60, v60, v86, v87
	s_nop 0
	v_max3_f32 v59, v59, v84, v85
	v_max3_f32 v60, v60, v106, v107
	s_nop 0
	v_max3_f32 v59, v59, v104, v105
	v_max3_f32 v60, v60, v90, v91
	s_nop 0
	v_max3_f32 v59, v59, v88, v89
	v_max3_f32 v60, v60, v110, v111
	s_nop 0
	v_max3_f32 v59, v59, v108, v109
	v_max3_f32 v60, v60, v94, v95
	s_nop 0
	v_max3_f32 v59, v59, v92, v93
	s_nop 0
	v_max_f32 v59, v59, v60
	s_nop 0
	v_mov_b32_e32 v60, v59
	s_nop 1
	v_permlane32_swap_b32_e32 v59, v60
	v_max_f32 v59, v59, v60
	s_nop 0
	v_cmp_lt_f32_e32 vcc, s30, v59
	s_cbranch_vccnz .LBB2_19
.LBB2_7:
	s_waitcnt lgkmcnt(14)
	v_mfma_f32_32x32x16_f16 v[0:15], v[140:143], v[176:179], v[0:15]
	v_pk_add_f16 v56, v56, v58
	s_andn2_b64 vcc, exec, s[16:17]
	v_pk_add_f16 v56, v57, v56
	s_cbranch_vccnz .LBB2_9
	v_fma_mix_f32 v188, v56, 1.0, v188 op_sel_hi:[1,0,0]
	v_fma_mix_f32 v192, v56, 1.0, v192 op_sel:[1,0,0] op_sel_hi:[1,0,0]
.LBB2_9:
	s_waitcnt lgkmcnt(12)
	v_mfma_f32_32x32x16_f16 v[16:31], v[140:143], v[172:175], v[16:31]
	v_exp_f32_e32 v96, v96
	v_exp_f32_e32 v97, v97
	v_exp_f32_e32 v98, v98
	v_add_u32_e32 v60, s29, v190
	ds_read_b128 v[56:59], v60
	ds_read_b128 v[176:179], v60 offset:512
	s_waitcnt lgkmcnt(12)
	v_mfma_f32_32x32x16_f16 v[0:15], v[136:139], v[64:67], v[0:15]
	v_exp_f32_e32 v99, v99
	v_exp_f32_e32 v100, v100
	v_exp_f32_e32 v101, v101
	ds_read_b128 v[172:175], v60 offset:2048
	ds_read_b128 v[168:171], v60 offset:2560
	s_waitcnt lgkmcnt(12)
	v_mfma_f32_32x32x16_f16 v[16:31], v[136:139], v[68:71], v[16:31]
	v_exp_f32_e32 v102, v102
	v_exp_f32_e32 v103, v103
	v_exp_f32_e32 v104, v104
	ds_read_b128 v[164:167], v60 offset:4096
	ds_read_b128 v[160:163], v60 offset:4608
	s_waitcnt lgkmcnt(12)
	v_mfma_f32_32x32x16_f16 v[0:15], v[132:135], v[76:79], v[0:15]
	v_exp_f32_e32 v105, v105
	v_exp_f32_e32 v106, v106
	v_exp_f32_e32 v107, v107
	ds_read_b128 v[156:159], v60 offset:6144
	ds_read_b128 v[152:155], v60 offset:6656
	s_waitcnt lgkmcnt(12)
	v_mfma_f32_32x32x16_f16 v[16:31], v[132:135], v[48:51], v[16:31]
	v_exp_f32_e32 v108, v108
	v_exp_f32_e32 v109, v109
	v_exp_f32_e32 v110, v110
	s_waitcnt lgkmcnt(10)
	v_mfma_f32_32x32x16_f16 v[0:15], v[128:131], v[72:75], v[0:15]
	s_waitcnt vmcnt(2) lgkmcnt(0)
	s_barrier
	v_exp_f32_e32 v111, v111
	v_exp_f32_e32 v80, v80
	v_exp_f32_e32 v81, v81
	s_waitcnt lgkmcnt(8)
	v_mfma_f32_32x32x16_f16 v[16:31], v[128:131], v[52:55], v[16:31]
	v_exp_f32_e32 v82, v82
	v_exp_f32_e32 v83, v83
	v_exp_f32_e32 v84, v84
	s_andn2_b64 vcc, exec, s[8:9]
	s_cbranch_vccnz .LBB2_11
	v_add_u32_e32 v64, s23, v184
	ds_read_b128 v[48:51], v64 offset:49248
	ds_read_b128 v[52:55], v64 offset:49216
	ds_read_b128 v[60:63], v64 offset:49184
	ds_read_b128 v[64:67], v64 offset:49152
	s_waitcnt lgkmcnt(3)
	v_pk_mul_f32 v[12:13], v[12:13], v[48:49]
	s_waitcnt lgkmcnt(2)
	v_pk_mul_f32 v[8:9], v[8:9], v[52:53]
	s_waitcnt lgkmcnt(1)
	v_pk_mul_f32 v[4:5], v[4:5], v[60:61]
	v_pk_mul_f32 v[14:15], v[14:15], v[50:51]
	v_pk_mul_f32 v[10:11], v[10:11], v[54:55]
	v_pk_mul_f32 v[6:7], v[6:7], v[62:63]
	s_waitcnt lgkmcnt(0)
	v_pk_mul_f32 v[2:3], v[2:3], v[66:67]
	v_pk_mul_f32 v[0:1], v[0:1], v[64:65]
	v_pk_mul_f32 v[28:29], v[28:29], v[48:49]
	v_pk_mul_f32 v[24:25], v[24:25], v[52:53]
	v_pk_mul_f32 v[20:21], v[20:21], v[60:61]
	v_pk_mul_f32 v[30:31], v[30:31], v[50:51]
	v_pk_mul_f32 v[26:27], v[26:27], v[54:55]
	v_pk_mul_f32 v[22:23], v[22:23], v[62:63]
	v_pk_mul_f32 v[18:19], v[18:19], v[66:67]
	v_pk_mul_f32 v[16:17], v[16:17], v[64:65]
.LBB2_11:
	s_add_i32 s33, s29, 0x2000
	s_cmpk_lg_i32 s29, 0x4000
	s_cselect_b32 s33, s33, 0
	v_add_u32_e32 v191, s31, v187
	ds_read_b64_tr_b16 v[148:149], v191 offset:24576
	ds_read_b64_tr_b16 v[150:151], v191 offset:25088
	s_waitcnt lgkmcnt(9)
	v_mfma_f32_32x32x16_f16 v[64:79], v[56:59], v[124:127], v[32:47]
	v_exp_f32_e32 v88, v88
	v_exp_f32_e32 v89, v89
	v_cvt_pk_f16_f32 v140, v96, v97
	v_cvt_pk_f16_f32 v141, v98, v99
	ds_read_b64_tr_b16 v[144:145], v191 offset:28672
	ds_read_b64_tr_b16 v[146:147], v191 offset:29184
	s_waitcnt lgkmcnt(10)
	v_mfma_f32_32x32x16_f16 v[48:63], v[176:179], v[124:127], v[32:47]
	v_exp_f32_e32 v90, v90
	v_exp_f32_e32 v91, v91
	v_pk_add_f16 v128, v140, v141
	v_cvt_pk_f16_f32 v142, v100, v101
	v_cvt_pk_f16_f32 v143, v102, v103
	ds_read_b64_tr_b16 v[96:97], v191 offset:25600
	ds_read_b64_tr_b16 v[98:99], v191 offset:26112
	s_waitcnt lgkmcnt(11)
	v_mfma_f32_32x32x16_f16 v[64:79], v[172:175], v[120:123], v[64:79]
	v_exp_f32_e32 v92, v92
	v_exp_f32_e32 v93, v93
	v_pk_add_f16 v129, v142, v143
	v_cvt_pk_f16_f32 v136, v104, v105
	v_cvt_pk_f16_f32 v137, v106, v107
	ds_read_b64_tr_b16 v[100:101], v191 offset:29696
	ds_read_b64_tr_b16 v[102:103], v191 offset:30208
	s_waitcnt lgkmcnt(12)
	v_mfma_f32_32x32x16_f16 v[48:63], v[168:171], v[120:123], v[48:63]
	v_exp_f32_e32 v94, v94
	v_exp_f32_e32 v95, v95
	v_pk_add_f16 v128, v128, v129
	v_cvt_pk_f16_f32 v138, v108, v109
	v_cvt_pk_f16_f32 v139, v110, v111
	v_pk_add_f16 v172, v136, v137
	s_min_u32 s31, s26, 27
	s_lshl_b32 s31, s31, 13
	s_add_u32 s31, s14, s31
	s_addc_u32 s35, s15, 0
	s_add_u32 s34, s31, 0x8000
	s_addc_u32 s35, s35, 0
	s_add_i32 s31, s29, s24
	s_mov_b32 s36, m0
	s_mov_b32 m0, s31
	s_nop 0
	global_load_lds_dwordx4 v189, s[34:35]
	s_mov_b32 m0, s36
	ds_read_b64_tr_b16 v[104:105], v191 offset:26624
	ds_read_b64_tr_b16 v[106:107], v191 offset:27136
	s_waitcnt lgkmcnt(13)
	v_mfma_f32_32x32x16_f16 v[64:79], v[164:167], v[116:119], v[64:79]
	v_pk_add_f16 v108, v138, v139
	v_cvt_pk_f16_f32 v132, v80, v81
	v_cvt_pk_f16_f32 v133, v82, v83
	v_exp_f32_e32 v85, v85
	v_exp_f32_e32 v86, v86
	ds_read_b64_tr_b16 v[80:81], v191 offset:30720
	ds_read_b64_tr_b16 v[82:83], v191 offset:31232
	s_waitcnt lgkmcnt(14)
	v_mfma_f32_32x32x16_f16 v[48:63], v[160:163], v[116:119], v[48:63]
	v_exp_f32_e32 v87, v87
	v_pk_add_f16 v129, v172, v108
	v_cvt_pk_f16_f32 v134, v84, v85
	v_cvt_pk_f16_f32 v135, v86, v87
	v_pk_add_f16 v164, v132, v133
	s_add_u32 s34, s27, 0x4000
	s_addc_u32 s35, s28, 0
	s_add_i32 s31, s33, s25
	s_mov_b32 s36, m0
	s_mov_b32 m0, s31
	s_nop 0
	global_load_lds_dwordx4 v189, s[34:35]
	s_mov_b32 m0, s36
	ds_read_b64_tr_b16 v[108:109], v191 offset:27648
	ds_read_b64_tr_b16 v[110:111], v191 offset:28160
	s_waitcnt lgkmcnt(14)
	v_mfma_f32_32x32x16_f16 v[64:79], v[156:159], v[112:115], v[64:79]
	v_pk_add_f16 v161, v128, v129
	v_cvt_pk_f16_f32 v128, v88, v89
	v_cvt_pk_f16_f32 v129, v90, v91
	v_pk_add_f16 v160, v134, v135
	ds_read_b64_tr_b16 v[84:85], v191 offset:31744
	ds_read_b64_tr_b16 v[86:87], v191 offset:32256
	v_mfma_f32_32x32x16_f16 v[48:63], v[152:155], v[112:115], v[48:63]
	v_pk_add_f16 v88, v128, v129
	v_pk_add_f16 v89, v164, v160
	v_cvt_pk_f16_f32 v130, v92, v93
	v_cvt_pk_f16_f32 v131, v94, v95
	s_and_b64 vcc, exec, s[16:17]
	v_pk_add_f16 v89, v161, v89
	v_pk_add_f16 v90, v130, v131
	s_cbranch_vccnz .LBB2_13
	v_pk_add_f16 v91, v88, v90
	v_max3_f32 v93, v64, v65, v48
	v_max3_f32 v94, v66, v67, v49
	s_mov_b64 s[8:9], 0
	v_pk_add_f16 v91, v89, v91
	s_nop 0
	v_cvt_f32_f16_e32 v92, v91
	v_cvt_f32_f16_sdwa v91, v91 dst_sel:DWORD dst_unused:UNUSED_PAD src0_sel:WORD_1
	v_add_f32_e32 v91, v91, v92
	v_add_f32_e32 v188, v188, v91
	v_max3_f32 v91, v93, v50, v51
	v_max3_f32 v92, v94, v70, v71
	s_nop 0
	v_max3_f32 v91, v91, v68, v69
	v_max3_f32 v92, v92, v54, v55
	s_nop 0
	v_max3_f32 v91, v91, v52, v53
	v_max3_f32 v92, v92, v74, v75
	s_nop 0
	v_max3_f32 v91, v91, v72, v73
	v_max3_f32 v92, v92, v58, v59
	s_nop 0
	v_max3_f32 v91, v91, v56, v57
	v_max3_f32 v92, v92, v78, v79
	s_nop 0
	v_max3_f32 v91, v91, v76, v77
	v_max3_f32 v92, v92, v62, v63
	s_nop 0
	v_max3_f32 v91, v91, v60, v61
	s_nop 0
	v_max_f32 v91, v91, v92
	s_nop 0
	v_mov_b32_e32 v92, v91
	s_nop 1
	v_permlane32_swap_b32_e32 v91, v92
	v_max_f32 v91, v91, v92
	s_nop 0
	v_cmp_lt_f32_e32 vcc, s30, v91
	s_cbranch_vccnz .LBB2_22
.LBB2_13:
	s_waitcnt lgkmcnt(14)
	v_mfma_f32_32x32x16_f16 v[0:15], v[140:143], v[148:151], v[0:15]
	v_pk_add_f16 v88, v88, v90
	s_and_b64 vcc, exec, s[18:19]
	v_pk_add_f16 v88, v89, v88
	s_cbranch_vccnz .LBB2_15
	v_fma_mix_f32 v188, v88, 1.0, v188 op_sel_hi:[1,0,0]
	v_fma_mix_f32 v192, v88, 1.0, v192 op_sel:[1,0,0] op_sel_hi:[1,0,0]
.LBB2_15:
	s_waitcnt lgkmcnt(12)
	v_mfma_f32_32x32x16_f16 v[16:31], v[140:143], v[144:147], v[16:31]
	v_exp_f32_e32 v64, v64
	v_exp_f32_e32 v65, v65
	v_exp_f32_e32 v66, v66
	v_add_u32_e32 v88, s33, v190
	ds_read_b128 v[172:175], v88
	ds_read_b128 v[168:171], v88 offset:512
	s_waitcnt lgkmcnt(12)
	v_mfma_f32_32x32x16_f16 v[0:15], v[136:139], v[96:99], v[0:15]
	v_exp_f32_e32 v67, v67
	v_exp_f32_e32 v68, v68
	v_exp_f32_e32 v69, v69
	ds_read_b128 v[164:167], v88 offset:2048
	ds_read_b128 v[160:163], v88 offset:2560
	s_waitcnt lgkmcnt(12)
	v_mfma_f32_32x32x16_f16 v[16:31], v[136:139], v[100:103], v[16:31]
	v_exp_f32_e32 v70, v70
	v_exp_f32_e32 v71, v71
	v_exp_f32_e32 v72, v72
	ds_read_b128 v[156:159], v88 offset:4096
	ds_read_b128 v[152:155], v88 offset:4608
	s_waitcnt lgkmcnt(12)
	v_mfma_f32_32x32x16_f16 v[0:15], v[132:135], v[104:107], v[0:15]
	v_exp_f32_e32 v73, v73
	v_exp_f32_e32 v74, v74
	v_exp_f32_e32 v75, v75
	ds_read_b128 v[148:151], v88 offset:6144
	ds_read_b128 v[144:147], v88 offset:6656
	s_waitcnt lgkmcnt(12)
	v_mfma_f32_32x32x16_f16 v[16:31], v[132:135], v[80:83], v[16:31]
	v_exp_f32_e32 v76, v76
	v_exp_f32_e32 v77, v77
	v_exp_f32_e32 v78, v78
	s_waitcnt lgkmcnt(10)
	v_mfma_f32_32x32x16_f16 v[0:15], v[128:131], v[108:111], v[0:15]
	s_waitcnt vmcnt(2) lgkmcnt(0)
	s_barrier
	v_exp_f32_e32 v79, v79
	v_exp_f32_e32 v48, v48
	v_exp_f32_e32 v49, v49
	s_waitcnt lgkmcnt(8)
	v_mfma_f32_32x32x16_f16 v[16:31], v[128:131], v[84:87], v[16:31]
	v_exp_f32_e32 v50, v50
	v_exp_f32_e32 v51, v51
	v_exp_f32_e32 v52, v52
	s_andn2_b64 vcc, exec, s[8:9]
	s_cbranch_vccnz .LBB2_17
	v_add_u32_e32 v92, s23, v184
	ds_read_b128 v[80:83], v92 offset:49248
	ds_read_b128 v[84:87], v92 offset:49216
	ds_read_b128 v[88:91], v92 offset:49152
	ds_read_b128 v[92:95], v92 offset:49184
	s_waitcnt lgkmcnt(3)
	v_pk_mul_f32 v[14:15], v[14:15], v[82:83]
	v_pk_mul_f32 v[12:13], v[12:13], v[80:81]
	s_waitcnt lgkmcnt(2)
	v_pk_mul_f32 v[10:11], v[10:11], v[86:87]
	v_pk_mul_f32 v[8:9], v[8:9], v[84:85]
	s_waitcnt lgkmcnt(0)
	v_pk_mul_f32 v[6:7], v[6:7], v[94:95]
	v_pk_mul_f32 v[4:5], v[4:5], v[92:93]
	v_pk_mul_f32 v[2:3], v[2:3], v[90:91]
	v_pk_mul_f32 v[0:1], v[0:1], v[88:89]
	v_pk_mul_f32 v[30:31], v[30:31], v[82:83]
	v_pk_mul_f32 v[28:29], v[28:29], v[80:81]
	v_pk_mul_f32 v[26:27], v[26:27], v[86:87]
	v_pk_mul_f32 v[24:25], v[24:25], v[84:85]
	v_pk_mul_f32 v[22:23], v[22:23], v[94:95]
	v_pk_mul_f32 v[20:21], v[20:21], v[92:93]
	v_pk_mul_f32 v[18:19], v[18:19], v[90:91]
	v_pk_mul_f32 v[16:17], v[16:17], v[88:89]

.LBB2_25:
	ds_read_b64_tr_b16 v[96:97], v187 offset:24576
	ds_read_b64_tr_b16 v[98:99], v187 offset:25088
	s_waitcnt lgkmcnt(9)
	v_mfma_f32_32x32x16_f16 v[80:95], v[172:175], v[124:127], v[32:47]
	v_exp_f32_e32 v56, v56
	v_exp_f32_e32 v57, v57
	v_cvt_pk_f16_f32 v140, v64, v65
	v_cvt_pk_f16_f32 v141, v66, v67
	ds_read_b64_tr_b16 v[64:65], v187 offset:28672
	ds_read_b64_tr_b16 v[66:67], v187 offset:29184
	s_waitcnt lgkmcnt(10)
	v_mfma_f32_32x32x16_f16 v[32:47], v[168:171], v[124:127], v[32:47]
	v_exp_f32_e32 v58, v58
	v_exp_f32_e32 v59, v59
	v_pk_add_f16 v100, v140, v141
	v_cvt_pk_f16_f32 v142, v68, v69
	v_cvt_pk_f16_f32 v143, v70, v71
	ds_read_b64_tr_b16 v[68:69], v187 offset:25600
	ds_read_b64_tr_b16 v[70:71], v187 offset:26112
	s_waitcnt lgkmcnt(11)
	v_mfma_f32_32x32x16_f16 v[80:95], v[164:167], v[120:123], v[80:95]
	v_exp_f32_e32 v60, v60
	v_exp_f32_e32 v61, v61
	v_pk_add_f16 v101, v142, v143
	v_cvt_pk_f16_f32 v136, v72, v73
	v_cvt_pk_f16_f32 v137, v74, v75
	ds_read_b64_tr_b16 v[72:73], v187 offset:29696
	ds_read_b64_tr_b16 v[74:75], v187 offset:30208
	s_waitcnt lgkmcnt(12)
	v_mfma_f32_32x32x16_f16 v[32:47], v[160:163], v[120:123], v[32:47]
	v_exp_f32_e32 v62, v62
	v_exp_f32_e32 v63, v63
	v_pk_add_f16 v102, v136, v137
	v_pk_add_f16 v100, v100, v101
	v_cvt_pk_f16_f32 v138, v76, v77
	v_cvt_pk_f16_f32 v139, v78, v79
	s_add_u32 s14, s14, 0x3e000
	s_addc_u32 s15, s15, 0
	s_cmp_lg_u32 0, -1
	s_cselect_b32 s16, 0, 0
	s_add_i32 s16, s16, s22
	s_add_i32 s17, s16, 0x2000
	s_mov_b32 s18, m0
	s_mov_b32 m0, s17
	s_nop 0
	global_load_lds_dwordx4 v189, s[14:15]
	s_mov_b32 m0, s18
	ds_read_b64_tr_b16 v[104:105], v187 offset:26624
	ds_read_b64_tr_b16 v[106:107], v187 offset:27136
	s_waitcnt lgkmcnt(13)
	v_mfma_f32_32x32x16_f16 v[80:95], v[156:159], v[116:119], v[80:95]
	v_pk_add_f16 v101, v138, v139
	v_cvt_pk_f16_f32 v132, v48, v49
	v_cvt_pk_f16_f32 v133, v50, v51
	v_exp_f32_e32 v53, v53
	v_exp_f32_e32 v54, v54
	ds_read_b64_tr_b16 v[76:77], v187 offset:30720
	ds_read_b64_tr_b16 v[78:79], v187 offset:31232
	s_waitcnt lgkmcnt(14)
	v_mfma_f32_32x32x16_f16 v[32:47], v[152:155], v[116:119], v[32:47]
	v_exp_f32_e32 v55, v55
	v_pk_add_f16 v49, v102, v101
	v_cvt_pk_f16_f32 v134, v52, v53
	v_cvt_pk_f16_f32 v135, v54, v55
	v_pk_add_f16 v48, v132, v133
	s_add_u32 s12, s12, 0x3e000
	s_addc_u32 s13, s13, 0
	s_add_i32 s16, s16, 0xa000
	s_mov_b32 s14, m0
	s_mov_b32 m0, s16
	s_nop 0
	global_load_lds_dwordx4 v189, s[12:13]
	s_mov_b32 m0, s14
	ds_read_b64_tr_b16 v[108:109], v187 offset:27648
	ds_read_b64_tr_b16 v[110:111], v187 offset:28160
	s_waitcnt lgkmcnt(14)
	v_mfma_f32_32x32x16_f16 v[80:95], v[148:151], v[112:115], v[80:95]
	v_pk_add_f16 v49, v100, v49
	v_cvt_pk_f16_f32 v128, v56, v57
	v_cvt_pk_f16_f32 v129, v58, v59
	v_pk_add_f16 v50, v134, v135
	ds_read_b64_tr_b16 v[100:101], v187 offset:31744
	ds_read_b64_tr_b16 v[102:103], v187 offset:32256
	v_mfma_f32_32x32x16_f16 v[32:47], v[144:147], v[112:115], v[32:47]
	v_pk_add_f16 v116, v128, v129
	v_pk_add_f16 v48, v48, v50
	v_cvt_pk_f16_f32 v130, v60, v61
	v_cvt_pk_f16_f32 v131, v62, v63
	s_and_b64 vcc, exec, s[2:3]
	v_pk_add_f16 v112, v49, v48
	v_pk_add_f16 v113, v130, v131
	s_cbranch_vccnz .LBB2_27
	v_pk_add_f16 v48, v116, v113
	v_max3_f32 v50, v80, v81, v32
	v_max3_f32 v51, v82, v83, v33
	s_mov_b32 s2, 0x41000000
	v_pk_add_f16 v48, v112, v48
	s_mov_b64 s[8:9], 0
	v_cvt_f32_f16_e32 v49, v48
	v_cvt_f32_f16_sdwa v48, v48 dst_sel:DWORD dst_unused:UNUSED_PAD src0_sel:WORD_1
	v_add_f32_e32 v48, v48, v49
	v_add_f32_e32 v188, v188, v48
	v_max3_f32 v48, v50, v34, v35
	v_max3_f32 v49, v51, v86, v87
	s_nop 0
	v_max3_f32 v48, v48, v84, v85
	v_max3_f32 v49, v49, v38, v39
	s_nop 0
	v_max3_f32 v48, v48, v36, v37
	v_max3_f32 v49, v49, v90, v91
	s_nop 0
	v_max3_f32 v48, v48, v88, v89
	v_max3_f32 v49, v49, v42, v43
	s_nop 0
	v_max3_f32 v48, v48, v40, v41
	v_max3_f32 v49, v49, v94, v95
	s_nop 0
	v_max3_f32 v48, v48, v92, v93
	v_max3_f32 v49, v49, v46, v47
	s_nop 0
	v_max3_f32 v48, v48, v44, v45
	s_nop 0
	v_max_f32 v48, v48, v49
	s_nop 0
	v_mov_b32_e32 v49, v48
	s_nop 1
	v_permlane32_swap_b32_e32 v48, v49
	v_max_f32 v48, v48, v49
	s_nop 0
	v_cmp_lt_f32_e32 vcc, s2, v48
	s_cbranch_vccnz .LBB2_34
.LBB2_27:
	s_waitcnt lgkmcnt(14)
	v_mfma_f32_32x32x16_f16 v[0:15], v[140:143], v[96:99], v[0:15]
	s_and_b64 vcc, exec, s[4:5]
	s_cbranch_vccnz .LBB2_29
	v_pk_add_f16 v48, v116, v113
	s_nop 0
	v_pk_add_f16 v48, v112, v48
	s_nop 0
	v_cvt_f32_f16_e32 v49, v48
	v_cvt_f32_f16_sdwa v48, v48 dst_sel:DWORD dst_unused:UNUSED_PAD src0_sel:WORD_1
	v_add_f32_e32 v48, v48, v49
	v_add_f32_e32 v188, v48, v188
.LBB2_29:
	s_waitcnt lgkmcnt(12)
	v_mfma_f32_32x32x16_f16 v[16:31], v[140:143], v[64:67], v[16:31]
	v_exp_f32_e32 v80, v80
	v_exp_f32_e32 v81, v81
	v_exp_f32_e32 v82, v82
	s_waitcnt lgkmcnt(10)
	v_mfma_f32_32x32x16_f16 v[0:15], v[136:139], v[68:71], v[0:15]
	v_exp_f32_e32 v83, v83
	v_exp_f32_e32 v84, v84
	v_exp_f32_e32 v85, v85
	s_waitcnt lgkmcnt(8)
	v_mfma_f32_32x32x16_f16 v[16:31], v[136:139], v[72:75], v[16:31]
	v_exp_f32_e32 v86, v86
	v_exp_f32_e32 v87, v87
	v_exp_f32_e32 v88, v88
	s_waitcnt lgkmcnt(6)
	v_mfma_f32_32x32x16_f16 v[0:15], v[132:135], v[104:107], v[0:15]
	v_exp_f32_e32 v89, v89
	v_exp_f32_e32 v90, v90
	v_exp_f32_e32 v91, v91
	s_waitcnt lgkmcnt(4)
	v_mfma_f32_32x32x16_f16 v[16:31], v[132:135], v[76:79], v[16:31]
	v_exp_f32_e32 v92, v92
	v_exp_f32_e32 v93, v93
	v_exp_f32_e32 v94, v94
	s_waitcnt lgkmcnt(2)
	v_mfma_f32_32x32x16_f16 v[0:15], v[128:131], v[108:111], v[0:15]
	s_waitcnt vmcnt(0) lgkmcnt(0)
	s_barrier
	v_exp_f32_e32 v95, v95
	v_exp_f32_e32 v32, v32
	v_exp_f32_e32 v33, v33
	s_waitcnt lgkmcnt(0)
	v_mfma_f32_32x32x16_f16 v[16:31], v[128:131], v[100:103], v[16:31]
	v_exp_f32_e32 v34, v34
	v_exp_f32_e32 v35, v35
	v_exp_f32_e32 v36, v36
	s_andn2_b64 vcc, exec, s[8:9]
	v_add_u32_e32 v48, s23, v184
	s_cbranch_vccnz .LBB2_31
	ds_read_b128 v[50:53], v48 offset:49248
	ds_read_b128 v[54:57], v48 offset:49216
	ds_read_b128 v[58:61], v48 offset:49184
	ds_read_b128 v[62:65], v48 offset:49152
	s_waitcnt lgkmcnt(3)
	v_pk_mul_f32 v[12:13], v[12:13], v[50:51]
	s_waitcnt lgkmcnt(2)
	v_pk_mul_f32 v[8:9], v[8:9], v[54:55]
	s_waitcnt lgkmcnt(1)
	v_pk_mul_f32 v[4:5], v[4:5], v[58:59]
	v_pk_mul_f32 v[14:15], v[14:15], v[52:53]
	v_pk_mul_f32 v[10:11], v[10:11], v[56:57]
	v_pk_mul_f32 v[6:7], v[6:7], v[60:61]
	s_waitcnt lgkmcnt(0)
	v_pk_mul_f32 v[2:3], v[2:3], v[64:65]
	v_pk_mul_f32 v[0:1], v[0:1], v[62:63]
	v_pk_mul_f32 v[28:29], v[28:29], v[50:51]
	v_pk_mul_f32 v[24:25], v[24:25], v[54:55]
	v_pk_mul_f32 v[20:21], v[20:21], v[58:59]
	v_pk_mul_f32 v[30:31], v[30:31], v[52:53]
	v_pk_mul_f32 v[26:27], v[26:27], v[56:57]
	v_pk_mul_f32 v[22:23], v[22:23], v[60:61]
	v_pk_mul_f32 v[18:19], v[18:19], v[64:65]
	v_pk_mul_f32 v[16:17], v[16:17], v[62:63]
.LBB2_31:
	v_exp_f32_e32 v37, v37
	v_exp_f32_e32 v38, v38
	v_exp_f32_e32 v39, v39
	v_add_f32_e32 v188, v188, v192
	v_exp_f32_e32 v49, v40
	v_add_f32_e32 v40, v80, v81
	v_add_f32_e32 v40, v40, v82
	v_add_f32_e32 v40, v40, v83
	v_add_f32_e32 v40, v40, v84
	v_exp_f32_e32 v62, v41
	v_exp_f32_e32 v63, v42
	v_exp_f32_e32 v64, v43
	v_exp_f32_e32 v65, v44
	v_exp_f32_e32 v66, v45
	v_exp_f32_e32 v67, v46
	v_exp_f32_e32 v68, v47
	v_add_f32_e32 v50, v40, v85
	v_cvt_pk_f16_f32 v40, v80, v81
	v_cvt_pk_f16_f32 v41, v82, v83
	v_cvt_pk_f16_f32 v42, v84, v85
	v_cvt_pk_f16_f32 v43, v86, v87
	ds_read_b64_tr_b16 v[44:45], v187 offset:32768
	ds_read_b64_tr_b16 v[46:47], v187 offset:33280
	v_add_f32_e32 v50, v50, v86
	v_add_f32_e32 v54, v50, v87
	ds_read_b64_tr_b16 v[50:51], v187 offset:33792
	ds_read_b64_tr_b16 v[52:53], v187 offset:34304
	s_waitcnt lgkmcnt(2)
	v_mfma_f32_32x32x16_f16 v[0:15], v[40:43], v[44:47], v[0:15]
	ds_read_b64_tr_b16 v[44:45], v187 offset:36864
	ds_read_b64_tr_b16 v[46:47], v187 offset:37376
	v_add_f32_e32 v54, v54, v88
	v_add_f32_e32 v69, v54, v89
	v_cvt_pk_f16_f32 v54, v88, v89
	v_cvt_pk_f16_f32 v55, v90, v91
	v_cvt_pk_f16_f32 v56, v92, v93
	v_cvt_pk_f16_f32 v57, v94, v95
	s_waitcnt lgkmcnt(0)
	v_mfma_f32_32x32x16_f16 v[16:31], v[40:43], v[44:47], v[16:31]
	v_add_f32_e32 v40, v69, v90
	v_add_f32_e32 v40, v40, v91
	v_add_f32_e32 v40, v40, v92
	v_add_f32_e32 v40, v40, v93
	ds_read_b64_tr_b16 v[58:59], v187 offset:37888
	ds_read_b64_tr_b16 v[60:61], v187 offset:38400
	v_add_f32_e32 v40, v40, v94
	v_add_f32_e32 v40, v40, v95
	v_mfma_f32_32x32x16_f16 v[0:15], v[54:57], v[50:53], v[0:15]
	v_add_f32_e32 v40, v40, v32
	v_add_f32_e32 v50, v40, v33
	v_cvt_pk_f16_f32 v40, v32, v33
	v_cvt_pk_f16_f32 v41, v34, v35
	v_cvt_pk_f16_f32 v42, v36, v37
	v_cvt_pk_f16_f32 v43, v38, v39
	ds_read_b64_tr_b16 v[44:45], v187 offset:34816
	ds_read_b64_tr_b16 v[46:47], v187 offset:35328
	s_waitcnt lgkmcnt(2)
	v_mfma_f32_32x32x16_f16 v[16:31], v[54:57], v[58:61], v[16:31]
	v_add_f32_e32 v32, v50, v34
	v_add_f32_e32 v50, v32, v35
	ds_read_b64_tr_b16 v[32:33], v187 offset:35840
	ds_read_b64_tr_b16 v[34:35], v187 offset:36352
	v_add_f32_e32 v36, v50, v36
	v_add_f32_e32 v36, v36, v37
	v_cvt_pk_f16_f32 v50, v49, v62
	v_cvt_pk_f16_f32 v51, v63, v64
	s_waitcnt lgkmcnt(2)
	v_mfma_f32_32x32x16_f16 v[0:15], v[40:43], v[44:47], v[0:15]
	ds_read_b64_tr_b16 v[44:45], v187 offset:38912
	ds_read_b64_tr_b16 v[46:47], v187 offset:39424
	v_cvt_pk_f16_f32 v52, v65, v66
	v_cvt_pk_f16_f32 v53, v67, v68
	ds_read_b64_tr_b16 v[54:55], v187 offset:39936
	ds_read_b64_tr_b16 v[56:57], v187 offset:40448
	v_add_f32_e32 v36, v36, v38
	v_add_f32_e32 v36, v36, v39
	v_add_f32_e32 v36, v36, v49
	s_waitcnt lgkmcnt(2)
	v_mfma_f32_32x32x16_f16 v[16:31], v[40:43], v[44:47], v[16:31]
	v_add_f32_e32 v36, v36, v62
	v_mfma_f32_32x32x16_f16 v[0:15], v[50:53], v[32:35], v[0:15]
	v_add_f32_e32 v32, v36, v63
	v_add_f32_e32 v32, v32, v64
	v_add_f32_e32 v32, v32, v65
	v_add_f32_e32 v32, v32, v66
	v_add_f32_e32 v32, v32, v67
	v_add_f32_e32 v32, v32, v68
	v_add_f32_e32 v32, v188, v32
	s_waitcnt lgkmcnt(0)
	v_mfma_f32_32x32x16_f16 v[16:31], v[50:53], v[54:57], v[16:31]
	v_mov_b32_e32 v33, v32
	s_nop 1
	v_permlane32_swap_b32_e32 v32, v33
	s_and_saveexec_b64 s[2:3], s[0:1]
	v_add_f32_e32 v32, v32, v33
	ds_write_b32 v186, v32 offset:49280
	s_or_b64 exec, exec, s[2:3]
	s_waitcnt lgkmcnt(0)
	ds_read_b128 v[32:35], v48 offset:49280
	ds_read_b128 v[36:39], v48 offset:49312
	s_lshl_b64 s[0:1], s[10:11], 2
	s_add_u32 s0, s6, s0
	s_addc_u32 s1, s7, s1
	s_waitcnt lgkmcnt(1)
	v_rcp_f32_e32 v40, v32
	v_rcp_f32_e32 v41, v33
	s_lshl_b32 s2, s20, 13
	v_rcp_f32_e32 v42, v34
	v_rcp_f32_e32 v43, v35
	s_waitcnt lgkmcnt(0)
	v_rcp_f32_e32 v44, v36
	ds_read_b128 v[32:35], v48 offset:49344
	v_rcp_f32_e32 v45, v37
	v_rcp_f32_e32 v46, v38
	v_rcp_f32_e32 v47, v39
	ds_read_b128 v[36:39], v48 offset:49376
	s_add_i32 s2, s2, 0
	v_lshlrev_b32_e32 v48, 2, v181
	v_add3_u32 v48, s2, v182, v48
	v_mul_f32_e32 v0, v0, v40
	v_mul_f32_e32 v16, v16, v40
	v_add_u32_e32 v40, 0xc800, v48
	ds_write2_b32 v40, v0, v16 offset1:32
	v_mul_f32_e32 v0, v1, v41
	v_mul_f32_e32 v1, v17, v41
	ds_write2_b32 v40, v0, v1 offset0:64 offset1:96
	v_mul_f32_e32 v0, v2, v42
	v_mul_f32_e32 v1, v18, v42
	ds_write2_b32 v40, v0, v1 offset0:128 offset1:160
	v_mul_f32_e32 v0, v3, v43
	v_mul_f32_e32 v1, v19, v43
	s_waitcnt lgkmcnt(4)
	v_rcp_f32_e32 v32, v32
	ds_write2_b32 v40, v0, v1 offset0:192 offset1:224
	v_mul_f32_e32 v0, v4, v44
	v_mul_f32_e32 v1, v20, v44
	v_add_u32_e32 v2, 0xd000, v48
	v_rcp_f32_e32 v33, v33
	ds_write2_b32 v2, v0, v1 offset1:32
	v_mul_f32_e32 v0, v5, v45
	v_mul_f32_e32 v1, v21, v45
	v_rcp_f32_e32 v34, v34
	ds_write2_b32 v2, v0, v1 offset0:64 offset1:96
	v_mul_f32_e32 v0, v6, v46
	v_mul_f32_e32 v1, v22, v46
	v_rcp_f32_e32 v35, v35
	ds_write2_b32 v2, v0, v1 offset0:128 offset1:160
	v_mul_f32_e32 v0, v7, v47
	v_mul_f32_e32 v1, v23, v47
	s_waitcnt lgkmcnt(7)
	v_rcp_f32_e32 v36, v36
	ds_write2_b32 v2, v0, v1 offset0:192 offset1:224
	v_mul_f32_e32 v0, v8, v32
	v_mul_f32_e32 v1, v24, v32
	v_add_u32_e32 v2, 0xd800, v48
	v_rcp_f32_e32 v37, v37
	ds_write2_b32 v2, v0, v1 offset1:32
	v_mul_f32_e32 v0, v9, v33
	v_mul_f32_e32 v1, v25, v33
	v_rcp_f32_e32 v38, v38
	ds_write2_b32 v2, v0, v1 offset0:64 offset1:96
	v_mul_f32_e32 v0, v10, v34
	v_mul_f32_e32 v1, v26, v34
	v_rcp_f32_e32 v39, v39
	ds_write2_b32 v2, v0, v1 offset0:128 offset1:160
	v_mul_f32_e32 v0, v11, v35
	v_mul_f32_e32 v1, v27, v35
	ds_write2_b32 v2, v0, v1 offset0:192 offset1:224
	v_mul_f32_e32 v0, v12, v36
	v_mul_f32_e32 v1, v28, v36
	v_add_u32_e32 v2, 0xe000, v48
	ds_write2_b32 v2, v0, v1 offset1:32
	v_mul_f32_e32 v0, v13, v37
	v_mul_f32_e32 v1, v29, v37
	ds_write2_b32 v2, v0, v1 offset0:64 offset1:96
	v_mul_f32_e32 v0, v14, v38
	v_mul_f32_e32 v1, v30, v38
	ds_write2_b32 v2, v0, v1 offset0:128 offset1:160
	v_mul_f32_e32 v0, v15, v39
	v_mul_f32_e32 v1, v31, v39
	v_and_b32_e32 v8, 0xf0, v185
	ds_write2_b32 v2, v0, v1 offset0:192 offset1:224
	v_add_u32_e32 v14, s2, v8
	s_waitcnt lgkmcnt(0)
	v_lshl_add_u32 v0, v183, 8, v14
	v_or_b32_e32 v15, 4, v183
	s_lshl_b32 s3, s21, 2
	ds_read_b128 v[0:3], v0 offset:51200
	v_lshl_add_u32 v4, v15, 8, v14
	s_add_u32 s0, s0, s3
	ds_read_b128 v[4:7], v4 offset:51200
	s_addc_u32 s1, s1, 0
	v_mov_b32_e32 v9, 0
	v_lshl_add_u64 v[10:11], s[0:1], 0, v[8:9]
	v_lshlrev_b32_e32 v8, 11, v183
	v_lshl_add_u64 v[12:13], v[10:11], 0, v[8:9]
	v_lshlrev_b32_e32 v8, 11, v15
	s_waitcnt lgkmcnt(1)
	global_store_dwordx4 v[12:13], v[0:3], off sc1
	v_or_b32_e32 v15, 12, v183
	s_nop 0
	v_lshl_add_u64 v[0:1], v[10:11], 0, v[8:9]
	s_waitcnt lgkmcnt(0)
	global_store_dwordx4 v[0:1], v[4:7], off sc1
	s_nop 1
	v_or_b32_e32 v4, 8, v183
	v_lshl_add_u32 v0, v4, 8, v14
	ds_read_b128 v[0:3], v0 offset:51200
	v_lshlrev_b32_e32 v8, 11, v4
	v_lshl_add_u32 v4, v15, 8, v14
	ds_read_b128 v[4:7], v4 offset:51200
	v_lshl_add_u64 v[12:13], v[10:11], 0, v[8:9]
	v_lshlrev_b32_e32 v8, 11, v15
	s_waitcnt lgkmcnt(1)
	global_store_dwordx4 v[12:13], v[0:3], off sc1
	v_or_b32_e32 v15, 20, v183
	s_nop 0
	v_lshl_add_u64 v[0:1], v[10:11], 0, v[8:9]
	s_waitcnt lgkmcnt(0)
	global_store_dwordx4 v[0:1], v[4:7], off sc1
	s_nop 1
	v_or_b32_e32 v4, 16, v183
	v_lshl_add_u32 v0, v4, 8, v14
	ds_read_b128 v[0:3], v0 offset:51200
	v_lshlrev_b32_e32 v8, 11, v4
	v_lshl_add_u32 v4, v15, 8, v14
	ds_read_b128 v[4:7], v4 offset:51200
	v_lshl_add_u64 v[12:13], v[10:11], 0, v[8:9]
	v_lshlrev_b32_e32 v8, 11, v15
	s_waitcnt lgkmcnt(1)
	global_store_dwordx4 v[12:13], v[0:3], off sc1
	v_or_b32_e32 v15, 28, v183
	s_nop 0
	v_lshl_add_u64 v[0:1], v[10:11], 0, v[8:9]
	s_waitcnt lgkmcnt(0)
	global_store_dwordx4 v[0:1], v[4:7], off sc1
	s_nop 1
	v_or_b32_e32 v4, 24, v183
	v_lshl_add_u32 v0, v4, 8, v14
	ds_read_b128 v[0:3], v0 offset:51200
	v_lshlrev_b32_e32 v8, 11, v4
	v_lshl_add_u32 v4, v15, 8, v14
	ds_read_b128 v[4:7], v4 offset:51200
	v_lshl_add_u64 v[12:13], v[10:11], 0, v[8:9]
	v_lshlrev_b32_e32 v8, 11, v15
	s_waitcnt lgkmcnt(1)
	global_store_dwordx4 v[12:13], v[0:3], off sc1
	s_nop 1
	v_lshl_add_u64 v[0:1], v[10:11], 0, v[8:9]
	s_waitcnt lgkmcnt(0)
	global_store_dwordx4 v[0:1], v[4:7], off sc1
	s_endpgm
